# baseline (speedup 1.0000x reference)
_Z6k_poolPKDF16_PKiS2_PKfS4_S4_Pf:
	s_load_dwordx8 s[4:11], s[0:1], 0x0
	s_load_dwordx4 s[20:23], s[0:1], 0x28
	v_mov_b32_e32 v61, 0
	s_ashr_i32 s3, s2, 31
	s_lshl_b64 s[12:13], s[2:3], 2
	v_lshrrev_b32_e32 v37, 4, v0
	v_bfe_u32 v1, v0, 3, 1
	s_waitcnt lgkmcnt(0)
	s_mov_b64 s[16:17], s[4:5]
	s_and_b32 s24, s2, 7
	v_and_b32_e32 v45, 31, v0
	s_lshl_b32 s24, s24, 2
	v_lshl_add_u32 v45, v45, 5, s24
	global_load_dword v43, v45, s[6:7]
	s_mov_b64 s[14:15], s[8:9]
	s_add_u32 s6, s6, s12
	s_addc_u32 s7, s7, s13
	s_lshl_b32 s12, s2, 9
	s_ashr_i32 s13, s12, 31
	s_lshl_b64 s[12:13], s[12:13], 2
	s_add_u32 s8, s8, s12
	v_add_u32_e32 v1, v1, v37
	s_addc_u32 s9, s9, s13
	v_lshlrev_b32_e32 v3, 2, v1
	global_load_dword v2, v3, s[8:9]
	global_load_dword v4, v3, s[8:9] offset:256
	global_load_dword v10, v3, s[8:9] offset:512
	global_load_dword v14, v3, s[8:9] offset:768
	global_load_dword v18, v3, s[8:9] offset:1024
	global_load_dword v24, v3, s[8:9] offset:1280
	v_min_u32_e32 v1, 63, v1
	v_lshlrev_b32_e32 v1, 2, v1
	global_load_dword v6, v3, s[8:9] offset:1536
	global_load_dword v8, v1, s[8:9] offset:1792
	v_and_b32_e32 v36, 15, v0
	v_mov_b32_e32 v13, 0
	v_lshlrev_b32_e32 v12, 4, v36
	v_lshlrev_b32_e32 v51, 4, v36
	v_lshl_add_u64 v[22:23], s[4:5], 0, v[12:13]
	v_mbcnt_lo_u32_b32 v1, -1, 0
	s_load_dwordx2 s[4:5], s[0:1], 0x20
	v_mbcnt_hi_u32_b32 v1, -1, v1
	v_and_b32_e32 v38, 63, v0
	v_and_b32_e32 v9, 56, v1
	v_lshlrev_b32_e32 v7, 2, v38
	v_cmp_eq_u32_e32 vcc, 56, v9
	s_load_dword s6, s[6:7], 0x0
	v_mov_b32_e32 v40, 0xfc00fc00
	v_cndmask_b32_e64 v9, 8, 0, vcc
	v_add_lshl_u32 v49, v9, v1, 2
	v_or_b32_e32 v41, 64, v37
	v_or_b32_e32 v46, 0x80, v37
	s_mov_b32 s3, 0xfc00
	v_or_b32_e32 v47, 0xc0, v37
	v_or_b32_e32 v48, 0x100, v37
	s_waitcnt vmcnt(7)
	v_lshl_add_u32 v3, v2, 8, v51
	s_waitcnt vmcnt(6)
	global_load_dwordx4 v[30:33], v3, s[16:17]
	v_lshl_add_u32 v3, v4, 8, v51
	s_waitcnt vmcnt(6)
	global_load_dwordx4 v[26:29], v3, s[16:17]
	v_lshl_add_u32 v3, v10, 8, v51
	s_waitcnt vmcnt(6)
	global_load_dwordx4 v[10:13], v3, s[16:17]
	v_lshl_add_u32 v3, v14, 8, v51
	s_waitcnt vmcnt(6)
	global_load_dwordx4 v[14:17], v3, s[16:17]
	v_lshl_add_u32 v3, v18, 8, v51
	s_waitcnt vmcnt(6)
	global_load_dwordx4 v[18:21], v3, s[16:17]
	v_lshl_add_u32 v3, v24, 8, v51
	global_load_dwordx4 v[2:5], v3, s[16:17]
	s_nop 0
	global_load_dword v39, v7, s[10:11]
	s_waitcnt lgkmcnt(0)
	global_load_dword v34, v7, s[4:5]
	global_load_dword v35, v7, s[4:5] offset:256
	s_waitcnt vmcnt(10)
	v_lshl_add_u32 v42, v6, 8, v51
	s_waitcnt vmcnt(9)
	v_lshl_add_u32 v44, v8, 8, v51
	global_load_dwordx4 v[22:25], v42, s[16:17]
	global_load_dwordx4 v[6:9], v44, s[16:17]
	global_load_dwordx2 v[62:63], v61, s[20:21]
	s_lshr_b32 s25, s2, 3
	v_and_b32_e32 v45, 31, v0
	v_lshrrev_b32_e32 v50, 3, v43
	v_lshl_add_u32 v50, v50, 5, v45
	s_nop 0
	v_readlane_b32 s26, v50, s25
	s_nop 0
	v_cmp_lt_u32_e32 vcc, s26, v50
	s_bcnt1_i32_b32 s27, vcc_lo
	s_cmp_lt_u32 s27, 16
	s_cbranch_scc1 .Lp_nohelp
	s_sub_u32 s28, 32, s27
	s_mov_b32 s29, 0
	s_or_b32 s30, s29, 0x800
	v_cmp_le_u32_e32 vcc, s30, v50
	s_bcnt1_i32_b32 s31, vcc_lo
	s_cmp_ge_u32 s31, s28
	s_cselect_b32 s29, s30, s29
	s_or_b32 s30, s29, 0x400
	v_cmp_le_u32_e32 vcc, s30, v50
	s_bcnt1_i32_b32 s31, vcc_lo
	s_cmp_ge_u32 s31, s28
	s_cselect_b32 s29, s30, s29
	s_or_b32 s30, s29, 0x200
	v_cmp_le_u32_e32 vcc, s30, v50
	s_bcnt1_i32_b32 s31, vcc_lo
	s_cmp_ge_u32 s31, s28
	s_cselect_b32 s29, s30, s29
	s_or_b32 s30, s29, 0x100
	v_cmp_le_u32_e32 vcc, s30, v50
	s_bcnt1_i32_b32 s31, vcc_lo
	s_cmp_ge_u32 s31, s28
	s_cselect_b32 s29, s30, s29
	s_or_b32 s30, s29, 0x80
	v_cmp_le_u32_e32 vcc, s30, v50
	s_bcnt1_i32_b32 s31, vcc_lo
	s_cmp_ge_u32 s31, s28
	s_cselect_b32 s29, s30, s29
	s_or_b32 s30, s29, 0x40
	v_cmp_le_u32_e32 vcc, s30, v50
	s_bcnt1_i32_b32 s31, vcc_lo
	s_cmp_ge_u32 s31, s28
	s_cselect_b32 s29, s30, s29
	s_or_b32 s30, s29, 0x20
	v_cmp_le_u32_e32 vcc, s30, v50
	s_bcnt1_i32_b32 s31, vcc_lo
	s_cmp_ge_u32 s31, s28
	s_cselect_b32 s29, s30, s29
	s_or_b32 s30, s29, 0x10
	v_cmp_le_u32_e32 vcc, s30, v50
	s_bcnt1_i32_b32 s31, vcc_lo
	s_cmp_ge_u32 s31, s28
	s_cselect_b32 s29, s30, s29
	s_or_b32 s30, s29, 0x8
	v_cmp_le_u32_e32 vcc, s30, v50
	s_bcnt1_i32_b32 s31, vcc_lo
	s_cmp_ge_u32 s31, s28
	s_cselect_b32 s29, s30, s29
	s_or_b32 s30, s29, 0x4
	v_cmp_le_u32_e32 vcc, s30, v50
	s_bcnt1_i32_b32 s31, vcc_lo
	s_cmp_ge_u32 s31, s28
	s_cselect_b32 s29, s30, s29
	s_or_b32 s30, s29, 0x2
	v_cmp_le_u32_e32 vcc, s30, v50
	s_bcnt1_i32_b32 s31, vcc_lo
	s_cmp_ge_u32 s31, s28
	s_cselect_b32 s29, s30, s29
	s_or_b32 s30, s29, 0x1
	v_cmp_le_u32_e32 vcc, s30, v50
	s_bcnt1_i32_b32 s31, vcc_lo
	s_cmp_ge_u32 s31, s28
	s_cselect_b32 s29, s30, s29
	v_cmp_eq_u32_e32 vcc, s29, v50
	s_ff1_i32_b32 s31, vcc_lo
	s_cmp_lt_i32 s31, 0
	s_cbranch_scc1 .Lp_nohelp
	v_readlane_b32 s30, v43, s31
	s_lshl_b32 s31, s31, 3
	s_lshr_b32 s24, s24, 2
	s_or_b32 s31, s31, s24
	s_cmp_le_u32 s30, 0x100
	s_cbranch_scc1 .Lp_nohelp
	v_readfirstlane_b32 s30, v0
	s_lshl_b32 s31, s31, 11
	s_lshr_b32 s30, s30, 6
	s_lshl_b32 s30, s30, 4
	s_add_u32 s31, s31, s30
	s_add_u32 s31, s31, 0x400
	s_add_u32 s14, s14, s31
	s_addc_u32 s15, s15, 0
	s_load_dwordx4 s[32:35], s[14:15], 0x0
	s_load_dwordx4 s[36:39], s[14:15], 0x100
	s_load_dwordx4 s[40:43], s[14:15], 0x200
	s_load_dwordx4 s[44:47], s[14:15], 0x300
	v_and_b32_e32 v59, 1, v0
	v_lshlrev_b32_e32 v59, 7, v59
	s_waitcnt lgkmcnt(0)
	v_writelane_b32 v53, s32, 0
	v_writelane_b32 v53, s33, 2
	v_writelane_b32 v53, s34, 4
	v_writelane_b32 v53, s35, 6
	v_writelane_b32 v53, s36, 8
	v_writelane_b32 v53, s37, 10
	v_writelane_b32 v53, s38, 12
	v_writelane_b32 v53, s39, 14
	v_writelane_b32 v53, s40, 16
	v_writelane_b32 v53, s41, 18
	v_writelane_b32 v53, s42, 20
	v_writelane_b32 v53, s43, 22
	v_writelane_b32 v53, s44, 24
	v_writelane_b32 v53, s45, 26
	v_writelane_b32 v53, s46, 28
	v_writelane_b32 v53, s47, 30
	s_nop 1
	v_mov_b32_dpp v58, v53 quad_perm:[0,0,2,2] row_mask:0xf bank_mask:0xf
	s_mov_b32 exec_hi, 0
	v_lshl_add_u32 v58, v58, 8, v59
	global_load_dword v60, v58, s[16:17]
	s_mov_b64 exec, -1
.Lp_nohelp:
	s_min_i32 s4, s6, 0x1ff
	s_waitcnt vmcnt(11)
	v_cmp_gt_i32_e32 vcc, s4, v37
	v_mov_b32_dpp v54, v30 row_shl:8 row_mask:0xf bank_mask:0xf bound_ctrl:0
	v_mov_b32_dpp v55, v31 row_shl:8 row_mask:0xf bank_mask:0xf bound_ctrl:0
	v_mov_b32_dpp v56, v32 row_shl:8 row_mask:0xf bank_mask:0xf bound_ctrl:0
	v_mov_b32_dpp v57, v33 row_shl:8 row_mask:0xf bank_mask:0xf bound_ctrl:0
	v_pk_add_f16 v30, v30, v54
	v_pk_add_f16 v31, v31, v55
	v_pk_add_f16 v32, v32, v56
	v_pk_add_f16 v33, v33, v57
	v_cndmask_b32_e32 v30, v40, v30, vcc
	v_cndmask_b32_e32 v31, v40, v31, vcc
	v_cndmask_b32_e32 v32, v40, v32, vcc
	v_cndmask_b32_e32 v33, v40, v33, vcc
	s_waitcnt vmcnt(10)
	v_cmp_gt_i32_e32 vcc, s4, v41
	v_mov_b32_dpp v54, v26 row_shl:8 row_mask:0xf bank_mask:0xf bound_ctrl:0
	v_mov_b32_dpp v55, v27 row_shl:8 row_mask:0xf bank_mask:0xf bound_ctrl:0
	v_mov_b32_dpp v56, v28 row_shl:8 row_mask:0xf bank_mask:0xf bound_ctrl:0
	v_mov_b32_dpp v57, v29 row_shl:8 row_mask:0xf bank_mask:0xf bound_ctrl:0
	v_pk_add_f16 v26, v26, v54
	v_pk_add_f16 v27, v27, v55
	v_pk_add_f16 v28, v28, v56
	v_pk_add_f16 v29, v29, v57
	v_cndmask_b32_e32 v26, v40, v26, vcc
	v_cndmask_b32_e32 v27, v40, v27, vcc
	v_cndmask_b32_e32 v28, v40, v28, vcc
	v_cndmask_b32_e32 v29, v40, v29, vcc
	v_pk_max_f16 v30, v30, v26
	v_pk_max_f16 v31, v31, v27
	v_pk_max_f16 v32, v32, v28
	v_pk_max_f16 v33, v33, v29
	s_waitcnt vmcnt(9)
	v_cmp_gt_i32_e32 vcc, s4, v46
	v_mov_b32_dpp v54, v10 row_shl:8 row_mask:0xf bank_mask:0xf bound_ctrl:0
	v_mov_b32_dpp v55, v11 row_shl:8 row_mask:0xf bank_mask:0xf bound_ctrl:0
	v_mov_b32_dpp v56, v12 row_shl:8 row_mask:0xf bank_mask:0xf bound_ctrl:0
	v_mov_b32_dpp v57, v13 row_shl:8 row_mask:0xf bank_mask:0xf bound_ctrl:0
	v_pk_add_f16 v10, v10, v54
	v_pk_add_f16 v11, v11, v55
	v_pk_add_f16 v12, v12, v56
	v_pk_add_f16 v13, v13, v57
	v_cndmask_b32_e32 v10, v40, v10, vcc
	v_cndmask_b32_e32 v11, v40, v11, vcc
	v_cndmask_b32_e32 v12, v40, v12, vcc
	v_cndmask_b32_e32 v13, v40, v13, vcc
	v_pk_max_f16 v30, v30, v10
	v_pk_max_f16 v31, v31, v11
	v_pk_max_f16 v32, v32, v12
	v_pk_max_f16 v33, v33, v13
	s_waitcnt vmcnt(8)
	v_cmp_gt_i32_e32 vcc, s4, v47
	v_mov_b32_dpp v54, v14 row_shl:8 row_mask:0xf bank_mask:0xf bound_ctrl:0
	v_mov_b32_dpp v55, v15 row_shl:8 row_mask:0xf bank_mask:0xf bound_ctrl:0
	v_mov_b32_dpp v56, v16 row_shl:8 row_mask:0xf bank_mask:0xf bound_ctrl:0
	v_mov_b32_dpp v57, v17 row_shl:8 row_mask:0xf bank_mask:0xf bound_ctrl:0
	v_pk_add_f16 v14, v14, v54
	v_pk_add_f16 v15, v15, v55
	v_pk_add_f16 v16, v16, v56
	v_pk_add_f16 v17, v17, v57
	v_cndmask_b32_e32 v14, v40, v14, vcc
	v_cndmask_b32_e32 v15, v40, v15, vcc
	v_cndmask_b32_e32 v16, v40, v16, vcc
	v_cndmask_b32_e32 v17, v40, v17, vcc
	v_pk_max_f16 v30, v30, v14
	v_pk_max_f16 v31, v31, v15
	v_pk_max_f16 v32, v32, v16
	v_pk_max_f16 v33, v33, v17
	s_waitcnt vmcnt(7)
	v_cmp_gt_i32_e32 vcc, s4, v48
	v_mov_b32_dpp v54, v18 row_shl:8 row_mask:0xf bank_mask:0xf bound_ctrl:0
	v_mov_b32_dpp v55, v19 row_shl:8 row_mask:0xf bank_mask:0xf bound_ctrl:0
	v_mov_b32_dpp v56, v20 row_shl:8 row_mask:0xf bank_mask:0xf bound_ctrl:0
	v_mov_b32_dpp v57, v21 row_shl:8 row_mask:0xf bank_mask:0xf bound_ctrl:0
	v_pk_add_f16 v18, v18, v54
	v_pk_add_f16 v19, v19, v55
	v_pk_add_f16 v20, v20, v56
	v_pk_add_f16 v21, v21, v57
	v_cndmask_b32_e32 v18, v40, v18, vcc
	v_cndmask_b32_e32 v19, v40, v19, vcc
	v_cndmask_b32_e32 v20, v40, v20, vcc
	v_cndmask_b32_e32 v21, v40, v21, vcc
	v_pk_max_f16 v30, v30, v18
	v_pk_max_f16 v31, v31, v19
	v_pk_max_f16 v32, v32, v20
	v_pk_max_f16 v33, v33, v21
	v_or_b32_e32 v52, 0x140, v37
	s_waitcnt vmcnt(6)
	v_cmp_gt_i32_e32 vcc, s4, v52
	v_mov_b32_dpp v54, v2 row_shl:8 row_mask:0xf bank_mask:0xf bound_ctrl:0
	v_mov_b32_dpp v55, v3 row_shl:8 row_mask:0xf bank_mask:0xf bound_ctrl:0
	v_mov_b32_dpp v56, v4 row_shl:8 row_mask:0xf bank_mask:0xf bound_ctrl:0
	v_mov_b32_dpp v57, v5 row_shl:8 row_mask:0xf bank_mask:0xf bound_ctrl:0
	v_pk_add_f16 v2, v2, v54
	v_pk_add_f16 v3, v3, v55
	v_pk_add_f16 v4, v4, v56
	v_pk_add_f16 v5, v5, v57
	v_cndmask_b32_e32 v2, v40, v2, vcc
	v_cndmask_b32_e32 v3, v40, v3, vcc
	v_cndmask_b32_e32 v4, v40, v4, vcc
	v_cndmask_b32_e32 v5, v40, v5, vcc
	v_pk_max_f16 v30, v30, v2
	v_pk_max_f16 v31, v31, v3
	v_pk_max_f16 v32, v32, v4
	v_pk_max_f16 v33, v33, v5
	v_or_b32_e32 v52, 0x180, v37
	s_waitcnt vmcnt(2)
	v_cmp_gt_i32_e32 vcc, s4, v52
	v_mov_b32_dpp v54, v22 row_shl:8 row_mask:0xf bank_mask:0xf bound_ctrl:0
	v_mov_b32_dpp v55, v23 row_shl:8 row_mask:0xf bank_mask:0xf bound_ctrl:0
	v_mov_b32_dpp v56, v24 row_shl:8 row_mask:0xf bank_mask:0xf bound_ctrl:0
	v_mov_b32_dpp v57, v25 row_shl:8 row_mask:0xf bank_mask:0xf bound_ctrl:0
	v_pk_add_f16 v22, v22, v54
	v_pk_add_f16 v23, v23, v55
	v_pk_add_f16 v24, v24, v56
	v_pk_add_f16 v25, v25, v57
	v_cndmask_b32_e32 v22, v40, v22, vcc
	v_cndmask_b32_e32 v23, v40, v23, vcc
	v_cndmask_b32_e32 v24, v40, v24, vcc
	v_cndmask_b32_e32 v25, v40, v25, vcc
	v_pk_max_f16 v30, v30, v22
	v_pk_max_f16 v31, v31, v23
	v_pk_max_f16 v32, v32, v24
	v_pk_max_f16 v33, v33, v25
	v_or_b32_e32 v52, 0x1c0, v37
	s_waitcnt vmcnt(1)
	v_cmp_gt_i32_e32 vcc, s4, v52
	v_mov_b32_dpp v54, v6 row_shl:8 row_mask:0xf bank_mask:0xf bound_ctrl:0
	v_mov_b32_dpp v55, v7 row_shl:8 row_mask:0xf bank_mask:0xf bound_ctrl:0
	v_mov_b32_dpp v56, v8 row_shl:8 row_mask:0xf bank_mask:0xf bound_ctrl:0
	v_mov_b32_dpp v57, v9 row_shl:8 row_mask:0xf bank_mask:0xf bound_ctrl:0
	v_pk_add_f16 v6, v6, v54
	v_pk_add_f16 v7, v7, v55
	v_pk_add_f16 v8, v8, v56
	v_pk_add_f16 v9, v9, v57
	v_cndmask_b32_e32 v6, v40, v6, vcc
	v_cndmask_b32_e32 v7, v40, v7, vcc
	v_cndmask_b32_e32 v8, v40, v8, vcc
	v_cndmask_b32_e32 v9, v40, v9, vcc
	v_pk_max_f16 v30, v30, v6
	v_pk_max_f16 v31, v31, v7
	v_pk_max_f16 v32, v32, v8
	v_pk_max_f16 v33, v33, v9
	v_mov_b32_e32 v54, v30
	v_mov_b32_e32 v55, v31
	v_mov_b32_e32 v56, v32
	v_mov_b32_e32 v57, v33
	v_lshlrev_b32_e32 v2, 2, v0
	s_nop 0
	v_permlane32_swap_b32_e32 v30, v54
	v_permlane32_swap_b32_e32 v31, v55
	v_permlane32_swap_b32_e32 v32, v56
	v_permlane32_swap_b32_e32 v33, v57
	v_pk_max_f16 v30, v30, v54
	v_pk_max_f16 v31, v31, v55
	v_pk_max_f16 v32, v32, v56
	v_pk_max_f16 v33, v33, v57
	v_mov_b32_e32 v54, v30
	v_mov_b32_e32 v55, v31
	v_mov_b32_e32 v56, v32
	v_mov_b32_e32 v57, v33
	s_nop 1
	v_permlane16_swap_b32_e32 v30, v54
	v_permlane16_swap_b32_e32 v31, v55
	v_permlane16_swap_b32_e32 v32, v56
	v_permlane16_swap_b32_e32 v33, v57
	v_pk_max_f16 v30, v30, v54
	v_pk_max_f16 v31, v31, v55
	v_pk_max_f16 v32, v32, v56
	v_pk_max_f16 v33, v33, v57
	v_cmp_gt_u32_e32 vcc, 8, v38
	s_and_saveexec_b64 s[4:5], vcc
	s_cbranch_execz .LBB2_2
	v_cvt_f32_f16_e32 v4, v30
	v_cvt_f32_f16_sdwa v5, v30 dst_sel:DWORD dst_unused:UNUSED_PAD src0_sel:WORD_1
	v_cvt_f32_f16_e32 v6, v31
	v_cvt_f32_f16_sdwa v7, v31 dst_sel:DWORD dst_unused:UNUSED_PAD src0_sel:WORD_1
	v_cvt_f32_f16_e32 v8, v32
	v_cvt_f32_f16_sdwa v9, v32 dst_sel:DWORD dst_unused:UNUSED_PAD src0_sel:WORD_1
	v_cvt_f32_f16_e32 v10, v33
	v_cvt_f32_f16_sdwa v11, v33 dst_sel:DWORD dst_unused:UNUSED_PAD src0_sel:WORD_1
	v_and_b32_e32 v3, 0xf00, v2
	v_lshl_add_u32 v3, v36, 5, v3
	ds_write_b128 v3, v[4:7]
	ds_write_b128 v3, v[8:11] offset:16

	.amdhsa_kernel _Z6k_poolPKDF16_PKiS2_PKfS4_S4_Pf
		.amdhsa_group_segment_fixed_size 4096
		.amdhsa_private_segment_fixed_size 0
		.amdhsa_kernarg_size 56
		.amdhsa_user_sgpr_count 2
		.amdhsa_user_sgpr_dispatch_ptr 0
		.amdhsa_user_sgpr_queue_ptr 0
		.amdhsa_user_sgpr_kernarg_segment_ptr 1
		.amdhsa_user_sgpr_dispatch_id 0
		.amdhsa_user_sgpr_kernarg_preload_length 0
		.amdhsa_user_sgpr_kernarg_preload_offset 0
		.amdhsa_user_sgpr_private_segment_size 0
		.amdhsa_uses_dynamic_stack 0
		.amdhsa_enable_private_segment 0
		.amdhsa_system_sgpr_workgroup_id_x 1
		.amdhsa_system_sgpr_workgroup_id_y 0
		.amdhsa_system_sgpr_workgroup_id_z 0
		.amdhsa_system_sgpr_workgroup_info 0
		.amdhsa_system_vgpr_workitem_id 0
		.amdhsa_next_free_vgpr 64
		.amdhsa_next_free_sgpr 48
		.amdhsa_accum_offset 64
		.amdhsa_reserve_vcc 1
		.amdhsa_float_round_mode_32 0
		.amdhsa_float_round_mode_16_64 0
		.amdhsa_float_denorm_mode_32 3
		.amdhsa_float_denorm_mode_16_64 3
		.amdhsa_dx10_clamp 1
		.amdhsa_ieee_mode 1
		.amdhsa_fp16_overflow 0
		.amdhsa_tg_split 0
		.amdhsa_exception_fp_ieee_invalid_op 0
		.amdhsa_exception_fp_denorm_src 0
		.amdhsa_exception_fp_ieee_div_zero 0
		.amdhsa_exception_fp_ieee_overflow 0
		.amdhsa_exception_fp_ieee_underflow 0
		.amdhsa_exception_fp_ieee_inexact 0
		.amdhsa_exception_int_div_zero 0
	.end_amdhsa_kernel

amdhsa.kernels:
  - .agpr_count:     0
    .args:
      - .actual_access:  read_only
        .address_space:  global
        .offset:         0
        .size:           8
        .value_kind:     global_buffer
      - .actual_access:  read_only
        .address_space:  global
        .offset:         8
        .size:           8
        .value_kind:     global_buffer
      - .actual_access:  write_only
        .address_space:  global
        .offset:         16
        .size:           8
        .value_kind:     global_buffer
      - .actual_access:  write_only
        .address_space:  global
        .offset:         24
        .size:           8
        .value_kind:     global_buffer
      - .actual_access:  write_only
        .address_space:  global
        .offset:         32
        .size:           8
        .value_kind:     global_buffer
      - .actual_access:  write_only
        .address_space:  global
        .offset:         40
        .size:           8
        .value_kind:     global_buffer
    .group_segment_fixed_size: 32
    .kernarg_segment_align: 8
    .kernarg_segment_size: 48
    .language:       OpenCL C
    .language_version:
      - 2
      - 0
    .max_flat_workgroup_size: 512
    .name:           _Z6k_prepPKiPKfPiS3_P15HIP_vector_typeIjLj4EEPh
    .private_segment_fixed_size: 0
    .sgpr_count:     16
    .sgpr_spill_count: 0
    .symbol:         _Z6k_prepPKiPKfPiS3_P15HIP_vector_typeIjLj4EEPh.kd
    .uniform_work_group_size: 1
    .uses_dynamic_stack: false
    .vgpr_count:     36
    .vgpr_spill_count: 0
    .wavefront_size: 64
  - .agpr_count:     0
    .args:
      - .actual_access:  read_only
        .address_space:  global
        .offset:         0
        .size:           8
        .value_kind:     global_buffer
      - .actual_access:  read_only
        .address_space:  global
        .offset:         8
        .size:           8
        .value_kind:     global_buffer
      - .actual_access:  read_only
        .address_space:  global
        .offset:         16
        .size:           8
        .value_kind:     global_buffer
      - .actual_access:  write_only
        .address_space:  global
        .offset:         24
        .size:           8
        .value_kind:     global_buffer
      - .actual_access:  read_only
        .address_space:  global
        .offset:         32
        .size:           8
        .value_kind:     global_buffer
    .group_segment_fixed_size: 16384
    .kernarg_segment_align: 8
    .kernarg_segment_size: 40
    .language:       OpenCL C
    .language_version:
      - 2
      - 0
    .max_flat_workgroup_size: 256
    .name:           _Z6k_gemmPKfS0_PK15HIP_vector_typeIjLj4EEPDF16_PKh
    .private_segment_fixed_size: 0
    .sgpr_count:     54
    .sgpr_spill_count: 0
    .symbol:         _Z6k_gemmPKfS0_PK15HIP_vector_typeIjLj4EEPDF16_PKh.kd
    .uniform_work_group_size: 1
    .uses_dynamic_stack: false
    .vgpr_count:     256
    .vgpr_spill_count: 0
    .wavefront_size: 64
  - .agpr_count:     0
    .args:
      - .actual_access:  read_only
        .address_space:  global
        .offset:         0
        .size:           8
        .value_kind:     global_buffer
      - .actual_access:  read_only
        .address_space:  global
        .offset:         8
        .size:           8
        .value_kind:     global_buffer
      - .actual_access:  read_only
        .address_space:  global
        .offset:         16
        .size:           8
        .value_kind:     global_buffer
      - .actual_access:  read_only
        .address_space:  global
        .offset:         24
        .size:           8
        .value_kind:     global_buffer
      - .actual_access:  read_only
        .address_space:  global
        .offset:         32
        .size:           8
        .value_kind:     global_buffer
      - .actual_access:  read_only
        .address_space:  global
        .offset:         40
        .size:           8
        .value_kind:     global_buffer
      - .actual_access:  write_only
        .address_space:  global
        .offset:         48
        .size:           8
        .value_kind:     global_buffer
    .group_segment_fixed_size: 4096
    .kernarg_segment_align: 8
    .kernarg_segment_size: 56
    .language:       OpenCL C
    .language_version:
      - 2
      - 0
    .max_flat_workgroup_size: 1024
    .name:           _Z6k_poolPKDF16_PKiS2_PKfS4_S4_Pf
    .private_segment_fixed_size: 0
    .sgpr_count:     54
    .sgpr_spill_count: 0
    .symbol:         _Z6k_poolPKDF16_PKiS2_PKfS4_S4_Pf.kd
    .uniform_work_group_size: 1
    .uses_dynamic_stack: false
    .vgpr_count:     64
    .vgpr_spill_count: 0
    .wavefront_size: 64
